# gridDim dwords cached in two spare SGPR-spill lanes (v_readlane instead of scalar loads inside every next-unit decode)
# baseline (speedup 1.0000x reference)
.LBB0_242:
	s_waitcnt lgkmcnt(0)
	v_readlane_b32 s0, v253, 1
	v_readlane_b32 s1, v253, 2
	s_add_u32 s64, s0, 0xe0
	s_addc_u32 s65, s1, 0
	s_load_dword s84, s[64:65], 0x0
	s_load_dword s85, s[64:65], 0x10
	s_waitcnt lgkmcnt(0)
	v_writelane_b32 v255, s84, 40
	v_writelane_b32 v255, s85, 41
	v_readlane_b32 s2, v253, 3
	v_readlane_b32 s3, v253, 4
	s_add_u32 s0, s2, 0x200
	s_addc_u32 s1, s3, 0
	v_writelane_b32 v253, s0, 5
	s_mov_b32 s83, 0
	s_mov_b32 s66, 2
	v_writelane_b32 v253, s1, 6
	s_add_u32 s0, s2, 0x1000
	s_addc_u32 s1, s3, 0
	v_writelane_b32 v253, s0, 7
	v_mov_b32_e32 v3, 0
	s_movk_i32 s67, 0x2000
	v_writelane_b32 v253, s1, 8
	s_add_u32 s0, s2, 0x1100
	s_addc_u32 s1, s3, 0
	v_writelane_b32 v253, s0, 9
	s_movk_i32 s68, 0x6000
	s_movk_i32 s69, 0x3000
	v_writelane_b32 v253, s1, 10
	s_add_u32 s0, s2, 0x1200
	s_addc_u32 s1, s3, 0
	v_writelane_b32 v253, s0, 11
	s_movk_i32 s70, 0x3600
	s_movk_i32 s71, 0x80
	v_writelane_b32 v253, s1, 12
	s_add_u32 s0, s2, 0x1300
	s_addc_u32 s1, s3, 0
	v_writelane_b32 v253, s0, 13
	s_cmp_eq_u32 s33, 15
	v_mov_b32_e32 v1, 0x4b000001
	v_writelane_b32 v253, s1, 14
	s_cselect_b64 s[0:1], -1, 0
	v_writelane_b32 v253, s0, 15
	s_cmp_eq_u32 s33, 14
	s_movk_i32 s72, 0x70
	v_writelane_b32 v253, s1, 16
	s_cselect_b64 s[0:1], -1, 0
	v_writelane_b32 v253, s0, 17
	s_cmp_eq_u32 s33, 13
	v_mov_b32_e32 v196, 1
	v_writelane_b32 v253, s1, 18
	s_cselect_b64 s[0:1], -1, 0
	v_writelane_b32 v253, s0, 19
	s_cmp_eq_u32 s33, 12
	v_mov_b32_e32 v252, 0x3727c5ac
	v_writelane_b32 v253, s1, 20
	s_cselect_b64 s[0:1], -1, 0
	v_writelane_b32 v253, s0, 21
	s_cmp_eq_u32 s33, 11
	v_mov_b32_e32 v199, 0x260
	v_writelane_b32 v253, s1, 22
	s_cselect_b64 s[0:1], -1, 0
	v_writelane_b32 v253, s0, 23
	s_cmp_eq_u32 s33, 10
	v_mov_b32_e32 v197, 0xff800000
	v_writelane_b32 v253, s1, 24
	s_cselect_b64 s[0:1], -1, 0
	v_writelane_b32 v253, s0, 25
	s_cmp_eq_u32 s33, 9
	v_mov_b32_e32 v198, 0x43e00000
	v_writelane_b32 v253, s1, 26
	s_cselect_b64 s[0:1], -1, 0
	v_writelane_b32 v253, s0, 27
	s_cmp_eq_u32 s33, 8
	v_mov_b32_e32 v200, 0x42000000
	v_writelane_b32 v253, s1, 28
	s_cselect_b64 s[0:1], -1, 0
	v_writelane_b32 v253, s0, 29
	s_cmp_eq_u32 s33, 7
	s_movk_i32 s74, 0x1ff
	v_writelane_b32 v253, s1, 30
	s_cselect_b64 s[0:1], -1, 0
	v_writelane_b32 v253, s0, 31
	s_cmp_eq_u32 s33, 6
	s_brev_b32 s75, -3
	v_writelane_b32 v253, s1, 32
	s_cselect_b64 s[0:1], -1, 0
	v_writelane_b32 v253, s0, 33
	s_cmp_eq_u32 s33, 5
	s_mov_b32 s76, 0x41000000
	v_writelane_b32 v253, s1, 34
	s_cselect_b64 s[0:1], -1, 0
	v_writelane_b32 v253, s0, 35
	s_cmp_eq_u32 s33, 4
	s_mov_b32 s78, 0xc3e00000
	v_writelane_b32 v253, s1, 36
	s_cselect_b64 s[0:1], -1, 0
	v_writelane_b32 v253, s0, 37
	s_cmp_eq_u32 s33, 3
	s_movk_i32 s79, 0x200
	v_writelane_b32 v253, s1, 38
	s_cselect_b64 s[0:1], -1, 0
	v_writelane_b32 v253, s0, 39
	s_cmp_eq_u32 s33, 2
	s_movk_i32 s80, 0xfdff
	v_writelane_b32 v253, s1, 40
	s_cselect_b64 s[0:1], -1, 0
	v_writelane_b32 v253, s0, 41
	s_cmp_eq_u32 s33, 1
	s_nop 0
	v_writelane_b32 v253, s1, 42
	s_cselect_b64 s[0:1], -1, 0
	v_writelane_b32 v253, s0, 43
	s_cmp_eq_u32 s33, 0
	s_nop 0
	v_writelane_b32 v253, s1, 44
	s_cselect_b64 s[0:1], -1, 0
	v_writelane_b32 v253, s0, 45
	s_nop 1
	v_writelane_b32 v253, s1, 46
	s_lshl_b32 s0, s33, 8
	s_add_u32 s0, s2, s0
	s_addc_u32 s1, s3, 0
	s_add_u32 s4, s0, 0x1400
	s_addc_u32 s5, s1, 0
	v_writelane_b32 v253, s4, 47
	s_nop 1
	v_writelane_b32 v253, s5, 48
	s_add_u32 s4, s2, 0xc900
	s_addc_u32 s5, s3, 0
	v_writelane_b32 v253, s4, 49
	s_nop 1
	v_writelane_b32 v253, s5, 50
	s_add_u32 s4, s2, 0x3400
	s_addc_u32 s5, s3, 0
	v_writelane_b32 v253, s4, 51
	s_add_u32 s2, s2, 0x3500
	s_addc_u32 s3, s3, 0
	v_writelane_b32 v253, s5, 52
	v_writelane_b32 v253, s2, 53
	s_add_u32 s0, s0, 0x2400
	s_addc_u32 s1, s1, 0
	v_writelane_b32 v253, s3, 54
	v_writelane_b32 v253, s0, 55
	s_add_i32 s73, 0, 0x27fc0
	s_add_i32 s50, 0, 0x27fc8
	v_writelane_b32 v253, s1, 56
	s_add_i32 s0, 0, 0x14000
	v_writelane_b32 v253, s0, 57
	s_add_i32 s0, 0, 0x18000
	v_writelane_b32 v253, s0, 58
	s_add_i32 s0, 0, 0x1c000
	v_writelane_b32 v253, s0, 59
	s_add_i32 s0, 0, 0x27ff0
	v_writelane_b32 v253, s0, 60
	s_add_i32 s0, 0, 0x27ff4
	v_writelane_b32 v253, s0, 61
	s_add_i32 s0, 0, 0x27ff8
	v_writelane_b32 v253, s0, 62
	s_add_i32 s0, 0, 0x27ffc
	v_writelane_b32 v253, s0, 63
	s_add_i32 s0, 0, 0x18900
	v_writelane_b32 v254, s0, 0
	s_add_i32 s0, 0, 0x22500
	v_writelane_b32 v254, s0, 1
	s_add_i32 s0, 0, 0x22580
	v_writelane_b32 v254, s0, 2
	s_add_i32 s0, 0, 0x21080
	v_writelane_b32 v254, s0, 3
	s_add_i32 s0, 0, 0x22000
	v_writelane_b32 v254, s0, 4
	s_mov_b64 s[0:1], -1
	v_writelane_b32 v254, s0, 5
	s_nop 1
	v_writelane_b32 v254, s1, 6
	s_mov_b32 s0, s83
	v_writelane_b32 v254, s0, 7
	s_nop 1
	v_writelane_b32 v254, s1, 8
	v_writelane_b32 v254, s64, 9
	s_nop 1
	v_writelane_b32 v254, s65, 10
	v_writelane_b32 v254, s73, 11
	v_writelane_b32 v254, s50, 12
	s_branch .LBB0_246

.LBB0_246:
	v_readlane_b32 s0, v253, 1
	v_readlane_b32 s1, v253, 2
	s_load_dword s2, s[0:1], 0xd8
	s_waitcnt lgkmcnt(0)
	s_cmp_lt_i32 s66, s2
	s_cbranch_scc1 .LBB0_402
	s_load_dword s44, s[0:1], 0xdc
	s_waitcnt lgkmcnt(0)
	s_cmp_gt_i32 s66, s44
	s_cbranch_scc1 .LBB0_402
	s_waitcnt vmcnt(0)
	v_mov_b32_e32 v4, v0
	v_readlane_b32 s15, v253, 0
	s_cmpk_lt_u32 s15, 0xd80
	v_readlane_b32 s4, v254, 7
	s_cselect_b64 s[2:3], -1, 0
	s_cmpk_gt_u32 s15, 0xd7f
	s_mul_i32 s10, s4, 0x6c0000
	v_readlane_b32 s5, v254, 8
	s_cbranch_scc1 .LBB0_250
	v_readlane_b32 s4, v255, 41
	v_readlane_b32 s6, v255, 40
	v_mov_b32_e32 v2, v0
	s_waitcnt lgkmcnt(0)
	s_lshr_b32 s4, s4, 16
	s_cmp_lg_u32 s4, 0
	s_cselect_b64 s[4:5], -1, 0
	s_cmp_lg_u64 s[4:5], 0
	s_addc_u32 s11, s6, s15
	s_lshr_b32 s5, s15, 3
	s_and_b32 s4, s15, 7
	s_add_i32 s6, s5, 0xffffff28
	s_cmpk_lt_u32 s15, 0x6c0
	s_cselect_b32 s5, s5, s6
	s_lshr_b32 s82, s5, 3
	s_cmpk_gt_u32 s15, 0x6bf
	s_waitcnt vmcnt(14)
	v_ashrrev_i32_e32 v6, 31, v2
	s_cselect_b32 s6, 8, 0
	s_and_b32 s5, s5, 7
	v_lshrrev_b32_e32 v6, 26, v6
	s_or_b32 s5, s5, s6
	v_lshlrev_b32_e32 v5, 4, v2
	v_add_u32_e32 v6, v2, v6
	v_bfe_i32 v2, v2, 27, 1
	s_lshl_b32 s5, s5, 3
	v_lshrrev_b32_e32 v2, 22, v2
	s_or_b32 s14, s5, s4
	v_add_u32_e32 v2, v5, v2
	s_load_dwordx2 s[4:5], s[0:1], 0xd0
	v_and_b32_e32 v2, 0xfffffc00, v2
	v_sub_u32_e32 v2, v5, v2
	v_lshrrev_b32_e32 v5, 4, v2
	v_bitop3_b32 v2, v5, v2, 32 bitop3:0x6c
	v_ashrrev_i32_e32 v7, 31, v2
	s_waitcnt lgkmcnt(0)
	s_add_u32 s6, s4, 0x22ac2000
	v_lshrrev_b32_e32 v7, 26, v7
	s_addc_u32 s7, s5, 0
	s_lshl_b64 s[8:9], s[82:83], 18
	v_add_u32_e32 v7, v2, v7
	s_add_u32 s4, s4, s8
	v_lshrrev_b32_e32 v8, 6, v7
	v_and_b32_e32 v7, 0xc0, v7
	s_addc_u32 s5, s5, s9
	v_ashrrev_i32_e32 v6, 6, v6
	v_sub_u32_e32 v2, v2, v7
	s_add_u32 s4, s4, s10
	v_lshlrev_b32_e32 v5, 3, v6
	v_lshlrev_b32_e32 v6, 5, v6
	v_ashrrev_i16_sdwa v2, v196, sext(v2) dst_sel:DWORD dst_unused:UNUSED_PAD src0_sel:DWORD src1_sel:BYTE_0
	s_addc_u32 s5, s5, 0
	v_and_b32_e32 v5, 0x3ffff0, v5
	v_and_b32_e32 v6, 32, v6
	v_bfe_i32 v2, v2, 0, 16
	s_add_u32 s4, s4, 0x1a2000
	s_addc_u32 s5, s5, 0
	s_lshl_b32 s8, s14, 18
	v_add_lshl_u32 v5, v8, v5, 10
	v_add_lshl_u32 v2, v6, v2, 1
	v_add3_u32 v180, v5, s8, v2
	v_add_u32_e32 v181, 0x10000, v180
	v_add_u32_e32 v182, 0x20000, v180
	v_add_u32_e32 v183, 0x30000, v180
	s_mov_b32 s16, s82
	s_mov_b32 s15, s11
	s_andn2_b64 vcc, exec, s[2:3]
	s_cbranch_vccz .LBB0_251
	s_branch .LBB0_307

.LBB0_259:
	ds_read_b128 v[20:23], v210
	ds_read_b128 v[24:27], v210 offset:1024
	ds_read_b128 v[28:31], v210 offset:2048
	ds_read_b128 v[32:35], v210 offset:3072
	ds_read_b128 v[4:7], v211
	ds_read_b128 v[8:11], v211 offset:1024
	ds_read_b128 v[12:15], v211 offset:2048
	ds_read_b128 v[16:19], v211 offset:3072
	s_add_u32 s2, s6, s12
	s_addc_u32 s3, s7, s13
	v_add_u32_e32 v192, 0xc000, v191
	s_add_u32 s2, s2, 0x80
	v_mov_b32_e32 v2, v182
	v_readfirstlane_b32 s26, v192
	v_add_u32_e32 v192, 0xe000, v191
	ds_read_b128 v[218:221], v214
	ds_read_b128 v[222:225], v214 offset:1024
	ds_read_b128 v[226:229], v215
	ds_read_b128 v[230:233], v215 offset:1024
	ds_read_b128 v[234:237], v216
	ds_read_b128 v[238:241], v216 offset:1024
	ds_read_b128 v[242:245], v217
	ds_read_b128 v[246:249], v217 offset:1024
	s_addc_u32 s3, s3, 0
	s_mov_b32 m0, s26
	v_readfirstlane_b32 s26, v192
	global_load_lds_dwordx4 v2, s[2:3]
	v_mov_b32_e32 v2, v183
	s_mov_b32 m0, s26
	s_nop 0
	global_load_lds_dwordx4 v2, s[2:3]
	s_waitcnt vmcnt(8)
	s_waitcnt lgkmcnt(0)
	s_barrier
	s_setprio 1
	s_waitcnt lgkmcnt(0)
	v_mfma_scale_f32_16x16x128_f8f6f4 v[176:179], v[20:27], v[218:225], v[176:179], v186, v185 op_sel_hi:[0,0,0]
	v_mfma_scale_f32_16x16x128_f8f6f4 v[172:175], v[28:35], v[218:225], v[172:175], v186, v185 op_sel_hi:[0,0,0]
	v_mfma_scale_f32_16x16x128_f8f6f4 v[168:171], v[20:27], v[226:233], v[168:171], v186, v185 op_sel_hi:[0,0,0]
	v_mfma_scale_f32_16x16x128_f8f6f4 v[164:167], v[28:35], v[226:233], v[164:167], v186, v185 op_sel_hi:[0,0,0]
	v_mfma_scale_f32_16x16x128_f8f6f4 v[160:163], v[20:27], v[234:241], v[160:163], v186, v185 op_sel_hi:[0,0,0]
	v_mfma_scale_f32_16x16x128_f8f6f4 v[156:159], v[28:35], v[234:241], v[156:159], v186, v185 op_sel_hi:[0,0,0]
	v_mfma_scale_f32_16x16x128_f8f6f4 v[152:155], v[20:27], v[242:249], v[152:155], v186, v185 op_sel_hi:[0,0,0]
	v_mfma_scale_f32_16x16x128_f8f6f4 v[148:151], v[28:35], v[242:249], v[148:151], v186, v185 op_sel_hi:[0,0,0]
	s_setprio 0
	s_setprio 1
	v_mfma_scale_f32_16x16x128_f8f6f4 v[112:115], v[4:11], v[218:225], v[112:115], v186, v185 op_sel_hi:[0,0,0]
	v_mfma_scale_f32_16x16x128_f8f6f4 v[108:111], v[12:19], v[218:225], v[108:111], v186, v185 op_sel_hi:[0,0,0]
	v_mfma_scale_f32_16x16x128_f8f6f4 v[104:107], v[4:11], v[226:233], v[104:107], v186, v185 op_sel_hi:[0,0,0]
	v_mfma_scale_f32_16x16x128_f8f6f4 v[100:103], v[12:19], v[226:233], v[100:103], v186, v185 op_sel_hi:[0,0,0]
	v_mfma_scale_f32_16x16x128_f8f6f4 v[96:99], v[4:11], v[234:241], v[96:99], v186, v185 op_sel_hi:[0,0,0]
	v_mfma_scale_f32_16x16x128_f8f6f4 v[92:95], v[12:19], v[234:241], v[92:95], v186, v185 op_sel_hi:[0,0,0]
	v_mfma_scale_f32_16x16x128_f8f6f4 v[88:91], v[4:11], v[242:249], v[88:91], v186, v185 op_sel_hi:[0,0,0]
	v_mfma_scale_f32_16x16x128_f8f6f4 v[84:87], v[12:19], v[242:249], v[84:87], v186, v185 op_sel_hi:[0,0,0]
	s_cmp_lg_u32 s25, 4
	s_setprio 0
	s_barrier
	s_cbranch_scc1 .LBB0_262
	s_cmpk_gt_u32 s15, 0xd7f
	s_mov_b64 s[20:21], 0
	s_cbranch_scc1 .LBB0_257
	v_readlane_b32 s2, v255, 41
	v_readlane_b32 s4, v255, 40
	v_mov_b32_e32 v2, v0
	s_mov_b64 s[20:21], -1
	v_ashrrev_i32_e32 v181, 31, v2
	v_lshrrev_b32_e32 v181, 26, v181
	v_lshlrev_b32_e32 v180, 4, v2
	v_add_u32_e32 v181, v2, v181
	v_bfe_i32 v2, v2, 27, 1
	s_waitcnt lgkmcnt(0)
	s_lshr_b32 s2, s2, 16
	v_lshrrev_b32_e32 v2, 22, v2
	s_cmp_lg_u32 s2, 0
	v_add_u32_e32 v2, v180, v2
	s_cselect_b64 s[2:3], -1, 0
	v_and_b32_e32 v2, 0xfffffc00, v2
	s_cmp_lg_u64 s[2:3], 0
	v_sub_u32_e32 v2, v180, v2
	s_addc_u32 s16, s4, s15
	s_lshr_b32 s3, s15, 3
	v_lshrrev_b32_e32 v180, 4, v2
	s_and_b32 s2, s15, 7
	s_add_i32 s4, s3, 0xffffff28
	v_bitop3_b32 v2, v180, v2, 32 bitop3:0x6c
	s_cmpk_lt_u32 s15, 0x6c0
	v_ashrrev_i32_e32 v182, 31, v2
	s_cselect_b32 s3, s3, s4
	s_cmpk_gt_u32 s15, 0x6bf
	v_lshrrev_b32_e32 v182, 26, v182
	s_cselect_b32 s4, 8, 0
	s_and_b32 s5, s3, 7
	v_add_u32_e32 v182, v2, v182
	s_or_b32 s4, s5, s4
	v_lshrrev_b32_e32 v183, 6, v182
	v_and_b32_e32 v182, 0xc0, v182
	s_lshr_b32 s82, s3, 3
	s_lshl_b32 s3, s4, 3
	v_ashrrev_i32_e32 v181, 6, v181
	v_sub_u32_e32 v2, v2, v182
	s_or_b32 s14, s3, s2
	v_lshlrev_b32_e32 v180, 3, v181
	v_lshlrev_b32_e32 v181, 5, v181
	v_ashrrev_i16_sdwa v2, v196, sext(v2) dst_sel:DWORD dst_unused:UNUSED_PAD src0_sel:DWORD src1_sel:BYTE_0
	s_lshl_b64 s[2:3], s[82:83], 18
	v_and_b32_e32 v180, 0x3ffff0, v180
	v_and_b32_e32 v181, 32, v181
	v_bfe_i32 v2, v2, 0, 16
	s_add_u32 s4, s19, s2
	s_addc_u32 s5, s22, s3
	s_lshl_b32 s2, s14, 18
	v_add_lshl_u32 v180, v183, v180, 10
	v_add_lshl_u32 v2, v181, v2, 1
	v_add3_u32 v180, v180, s2, v2
	v_add_u32_e32 v181, 0x10000, v180
	v_add_u32_e32 v182, 0x20000, v180
	v_add_u32_e32 v183, 0x30000, v180
	s_mov_b64 s[6:7], s[8:9]
	s_mov_b32 s15, s16
	s_mov_b32 s16, s82
	s_branch .LBB0_257

.LBB0_307:
	v_readlane_b32 s2, v255, 41
	v_readlane_b32 s33, v255, 40
	s_waitcnt lgkmcnt(0)
	s_lshr_b32 s2, s2, 16
	s_cmp_lg_u32 s2, 0
	s_cselect_b64 s[2:3], -1, 0
	s_cmp_lg_u64 s[2:3], 0
	s_addc_u32 s2, s33, 0
	s_cmpk_lg_i32 s2, 0x100
	s_cbranch_scc1 .LBB0_326
	v_readlane_b32 s2, v253, 0
	s_cmpk_lt_u32 s2, 0x80
	s_cbranch_scc1 .LBB0_326
	s_load_dwordx2 s[2:3], s[0:1], 0xd0
	v_readlane_b32 s4, v254, 7
	v_readlane_b32 s5, v254, 8
	s_lshl_b32 s82, s4, 6
	s_mov_b32 s6, s4
	s_lshl_b64 s[4:5], s[82:83], 2
	s_waitcnt lgkmcnt(0)
	s_add_u32 s4, s2, s4
	s_addc_u32 s5, s3, s5
	s_add_u32 s4, s4, 0xc800
	s_addc_u32 s5, s5, 0
	s_lshl_b32 s38, s6, 5
	s_add_u32 s39, s2, 0x126a2000
	s_addc_u32 s40, s3, 0
	s_add_u32 s41, s2, 0x26a2000
	s_addc_u32 s42, s3, 0
	s_mov_b32 s43, 3
	s_branch .LBB0_312

.LBB0_894:
	v_readlane_b32 s0, v253, 1
	v_readlane_b32 s1, v253, 2
	s_load_dword s2, s[0:1], 0xd8
	s_add_i32 s14, s66, 3
	s_waitcnt lgkmcnt(0)
	s_cmp_lt_i32 s14, s2
	s_cbranch_scc1 .LBB0_998
	s_load_dword s15, s[0:1], 0xdc
	s_waitcnt lgkmcnt(0)
	s_cmp_gt_i32 s14, s15
	s_cbranch_scc1 .LBB0_998
	s_waitcnt vmcnt(0)
	v_mov_b32_e32 v4, v0
	v_readlane_b32 s10, v253, 0
	s_cmpk_gt_u32 s10, 0x1ff
	s_cbranch_scc1 .LBB0_922
	v_bfe_i32 v7, v4, 27, 1
	v_lshlrev_b32_e32 v6, 4, v4
	v_lshrrev_b32_e32 v7, 22, v7
	v_add_u32_e32 v7, v6, v7
	v_and_b32_e32 v7, 0xfffffc00, v7
	v_sub_u32_e32 v7, v6, v7
	v_ashrrev_i32_e32 v2, 31, v4
	v_lshrrev_b32_e32 v8, 4, v7
	v_lshrrev_b32_e32 v2, 26, v2
	v_bitop3_b32 v7, v8, v7, 32 bitop3:0x6c
	v_add_u32_e32 v2, v4, v2
	v_ashrrev_i32_e32 v9, 31, v7
	v_ashrrev_i32_e32 v2, 6, v2
	v_lshrrev_b32_e32 v9, 26, v9
	v_lshlrev_b32_e32 v8, 3, v2
	v_add_u32_e32 v9, v7, v9
	v_and_b32_e32 v8, -16, v8
	v_ashrrev_i32_e32 v10, 6, v9
	v_add_u32_e32 v8, v10, v8
	v_and_b32_e32 v9, 0xc0, v9
	v_and_b32_e32 v10, 3, v10
	s_mov_b32 s2, 0x7fffe0
	v_sub_u32_e32 v7, v7, v9
	v_lshlrev_b32_e32 v9, 1, v8
	v_lshrrev_b32_e32 v11, 2, v8
	v_and_or_b32 v8, v8, s2, v10
	v_readlane_b32 s11, v255, 40
	v_readlane_b32 s2, v255, 41
	s_lshr_b32 s3, s10, 3
	v_lshlrev_b32_e32 v2, 5, v2
	v_ashrrev_i16_sdwa v7, v196, sext(v7) dst_sel:DWORD dst_unused:UNUSED_PAD src0_sel:DWORD src1_sel:BYTE_0
	s_sub_i32 s4, s3, 32
	s_waitcnt lgkmcnt(0)
	s_lshr_b32 s12, s2, 16
	s_and_b32 s2, s10, 7
	v_and_b32_e32 v2, 32, v2
	v_bfe_i32 v7, v7, 0, 16
	s_cmpk_lt_u32 s10, 0x100
	v_and_b32_e32 v9, 24, v9
	v_and_b32_e32 v11, 4, v11
	v_add_lshl_u32 v2, v2, v7, 1
	s_cselect_b32 s3, s3, s4
	s_lshr_b32 s4, s10, 5
	v_mov_b32_e32 v7, v0
	v_or3_b32 v8, v8, v9, v11
	s_lshr_b32 s20, s3, 3
	s_and_b32 s4, s4, 8
	s_and_b32 s3, s3, 7
	s_or_b32 s3, s3, s4
	v_ashrrev_i32_e32 v9, 31, v7
	v_lshrrev_b32_e32 v9, 26, v9
	v_lshl_add_u32 v2, v8, 9, v2
	s_lshl_b32 s3, s3, 3
	v_lshlrev_b32_e32 v8, 4, v7
	v_add_u32_e32 v9, v7, v9
	v_bfe_i32 v7, v7, 27, 1
	s_or_b32 s26, s3, s2
	v_lshrrev_b32_e32 v7, 22, v7
	s_load_dwordx2 s[2:3], s[0:1], 0xd0
	v_add_u32_e32 v7, v8, v7
	v_and_b32_e32 v7, 0xfffffc00, v7
	v_sub_u32_e32 v7, v8, v7
	v_lshrrev_b32_e32 v8, 4, v7
	v_bitop3_b32 v7, v8, v7, 32 bitop3:0x6c
	s_waitcnt lgkmcnt(0)
	s_add_u32 s4, s2, 0x41ac2000
	v_ashrrev_i32_e32 v10, 31, v7
	s_addc_u32 s5, s3, 0
	v_lshrrev_b32_e32 v10, 26, v10
	s_add_u32 s16, s2, 0x1ca2000
	s_mov_b32 s21, s83
	v_readlane_b32 s8, v254, 7
	v_add_u32_e32 v10, v7, v10
	s_addc_u32 s17, s3, 0
	s_lshl_b64 s[6:7], s[20:21], 17
	s_mul_i32 s8, s8, 0x180000
	v_lshrrev_b32_e32 v11, 6, v10
	v_and_b32_e32 v10, 0xc0, v10
	v_readlane_b32 s9, v254, 8
	s_add_u32 s8, s16, s8
	v_ashrrev_i32_e32 v9, 6, v9
	v_sub_u32_e32 v7, v7, v10
	s_addc_u32 s9, s17, 0
	v_lshlrev_b32_e32 v8, 3, v9
	v_lshlrev_b32_e32 v9, 5, v9
	v_ashrrev_i16_sdwa v7, v196, sext(v7) dst_sel:DWORD dst_unused:UNUSED_PAD src0_sel:DWORD src1_sel:BYTE_0
	s_add_u32 s6, s8, s6
	v_and_b32_e32 v8, 0x7ffff0, v8
	v_and_b32_e32 v9, 32, v9
	v_bfe_i32 v7, v7, 0, 16
	s_addc_u32 s7, s9, s7
	s_add_i32 s13, 0, 0x10000
	s_lshl_b32 s8, s26, 17
	v_add_lshl_u32 v8, v11, v8, 9
	v_add_lshl_u32 v7, v9, v7, 1
	v_add_u32_e32 v168, s13, v6
	v_add3_u32 v173, v8, s8, v7
	v_mov_b32_e32 v166, 0x7a7a7a7a
	v_mov_b32_e32 v167, 0x7b7b7b7b
	v_mov_b32_e32 v7, v2
	v_readfirstlane_b32 s8, v168
	v_add_u32_e32 v169, 0x2000, v168
	s_mov_b32 m0, s8
	s_add_u32 s8, s6, 0x8000
	v_readfirstlane_b32 s18, v169
	global_load_lds_dwordx4 v7, s[6:7]
	s_addc_u32 s9, s7, 0
	v_mov_b32_e32 v7, v2
	s_mov_b32 m0, s18
	v_add_u32_e32 v172, 0, v6
	global_load_lds_dwordx4 v7, s[8:9]
	v_readlane_b32 s8, v253, 57
	v_mov_b32_e32 v7, v2
	v_add_u32_e32 v175, 0x8000, v173
	v_add_u32_e32 v170, s8, v6
	s_add_u32 s8, s6, 0x10000
	v_readfirstlane_b32 s18, v170
	s_addc_u32 s9, s7, 0
	s_mov_b32 m0, s18
	v_add_u32_e32 v171, 0x2000, v170
	global_load_lds_dwordx4 v7, s[8:9]
	s_add_u32 s8, s6, 0x18000
	v_mov_b32_e32 v7, v2
	v_readfirstlane_b32 s18, v171
	s_addc_u32 s9, s7, 0
	s_mov_b32 m0, s18
	v_add_u32_e32 v174, 0x2000, v172
	global_load_lds_dwordx4 v7, s[8:9]
	v_mov_b32_e32 v7, v173
	v_readfirstlane_b32 s8, v172
	s_mov_b32 m0, s8
	v_readfirstlane_b32 s8, v174
	global_load_lds_dwordx4 v7, s[4:5]
	v_mov_b32_e32 v7, v175
	v_add_u32_e32 v176, 0x10000, v173
	s_mov_b32 m0, s8
	v_add_u32_e32 v177, 0x4000, v172
	global_load_lds_dwordx4 v7, s[4:5]
	v_mov_b32_e32 v7, v176
	v_readfirstlane_b32 s8, v177
	v_add_u32_e32 v179, 0x6000, v172
	v_add_u32_e32 v178, 0x18000, v173
	s_mov_b32 m0, s8
	v_readfirstlane_b32 s8, v179
	global_load_lds_dwordx4 v7, s[4:5]
	v_mov_b32_e32 v7, v178
	s_mov_b32 m0, s8
	v_ashrrev_i32_e32 v5, 8, v4
	global_load_lds_dwordx4 v7, s[4:5]
	v_cmp_eq_u32_e64 s[36:37], 1, v5
	s_and_saveexec_b64 s[8:9], s[36:37]
	s_cbranch_execz .LBB0_899
	s_barrier

.LBB0_998:
	v_readlane_b32 s0, v253, 1
	v_readlane_b32 s1, v253, 2
	s_load_dword s2, s[0:1], 0xd8
	s_add_i32 s14, s66, 4
	v_readlane_b32 s50, v254, 12
	s_mov_b32 s51, 0xf800000
	s_mov_b64 s[52:53], 0x80
	s_waitcnt lgkmcnt(0)
	s_cmp_lt_i32 s14, s2
	s_mov_b32 s54, 0x3d800000
	s_cbranch_scc1 .LBB0_1101
	s_load_dword s15, s[0:1], 0xdc
	s_waitcnt lgkmcnt(0)
	s_cmp_gt_i32 s14, s15
	s_cbranch_scc1 .LBB0_1101
	v_mov_b32_e32 v2, v0
	v_readlane_b32 s12, v253, 0
	s_cmpk_gt_u32 s12, 0x1ff
	s_cbranch_scc1 .LBB0_1025
	s_waitcnt vmcnt(0)
	v_bfe_i32 v7, v2, 27, 1
	v_lshlrev_b32_e32 v5, 4, v2
	v_lshrrev_b32_e32 v7, 22, v7
	v_add_u32_e32 v7, v5, v7
	v_and_b32_e32 v7, 0xfffffc00, v7
	v_sub_u32_e32 v7, v5, v7
	v_ashrrev_i32_e32 v6, 31, v2
	v_lshrrev_b32_e32 v8, 4, v7
	v_lshrrev_b32_e32 v6, 26, v6
	v_bitop3_b32 v7, v8, v7, 32 bitop3:0x6c
	v_add_u32_e32 v6, v2, v6
	v_ashrrev_i32_e32 v9, 31, v7
	v_ashrrev_i32_e32 v6, 6, v6
	v_lshrrev_b32_e32 v9, 26, v9
	v_lshlrev_b32_e32 v8, 3, v6
	v_add_u32_e32 v9, v7, v9
	v_and_b32_e32 v8, -16, v8
	v_ashrrev_i32_e32 v10, 6, v9
	v_add_u32_e32 v8, v10, v8
	v_and_b32_e32 v9, 0xc0, v9
	v_and_b32_e32 v10, 3, v10
	s_mov_b32 s2, 0x3fffe0
	v_sub_u32_e32 v7, v7, v9
	v_lshlrev_b32_e32 v9, 1, v8
	v_lshrrev_b32_e32 v11, 2, v8
	v_and_or_b32 v8, v8, s2, v10
	v_readlane_b32 s13, v255, 40
	v_readlane_b32 s2, v255, 41
	v_lshlrev_b32_e32 v6, 5, v6
	v_ashrrev_i16_sdwa v7, v196, sext(v7) dst_sel:DWORD dst_unused:UNUSED_PAD src0_sel:DWORD src1_sel:BYTE_0
	v_and_b32_e32 v6, 32, v6
	v_bfe_i32 v7, v7, 0, 16
	v_and_b32_e32 v9, 24, v9
	v_and_b32_e32 v11, 4, v11
	v_or3_b32 v8, v8, v9, v11
	v_add_lshl_u32 v6, v6, v7, 1
	s_lshr_b32 s3, s12, 3
	v_lshl_add_u32 v201, v8, 10, v6
	s_waitcnt lgkmcnt(0)
	s_lshr_b32 s18, s2, 16
	s_and_b32 s2, s12, 7
	s_sub_i32 s4, s3, 32
	v_mov_b32_e32 v6, v0
	s_cmpk_lt_u32 s12, 0x100
	s_cselect_b32 s3, s3, s4
	v_ashrrev_i32_e32 v8, 31, v6
	s_lshr_b32 s4, s12, 5
	v_lshrrev_b32_e32 v8, 26, v8
	s_lshr_b32 s6, s3, 3
	s_and_b32 s4, s4, 8
	s_and_b32 s3, s3, 7
	v_lshlrev_b32_e32 v7, 4, v6
	v_add_u32_e32 v8, v6, v8
	v_bfe_i32 v6, v6, 27, 1
	s_or_b32 s3, s3, s4
	v_lshrrev_b32_e32 v6, 22, v6
	s_load_dwordx2 s[4:5], s[0:1], 0xd0
	v_add_u32_e32 v6, v7, v6
	v_and_b32_e32 v6, 0xfffffc00, v6
	s_lshl_b32 s3, s3, 3
	v_sub_u32_e32 v6, v7, v6
	s_or_b32 s16, s3, s2
	v_lshrrev_b32_e32 v7, 4, v6
	v_bitop3_b32 v6, v7, v6, 32 bitop3:0x6c
	s_waitcnt lgkmcnt(0)
	s_add_u32 s8, s4, 0x49bc2000
	s_mov_b32 s7, s83
	v_readlane_b32 s10, v254, 7
	v_ashrrev_i32_e32 v9, 31, v6
	s_addc_u32 s9, s5, 0
	s_lshl_b64 s[2:3], s[6:7], 18
	s_lshl_b32 s7, s10, 20
	v_lshrrev_b32_e32 v9, 26, v9
	s_add_u32 s7, s4, s7
	v_add_u32_e32 v9, v6, v9
	s_addc_u32 s10, s5, 0
	v_lshrrev_b32_e32 v10, 6, v9
	v_and_b32_e32 v9, 0xc0, v9
	s_add_u32 s7, s7, 0x22a2000
	v_ashrrev_i32_e32 v8, 6, v8
	v_sub_u32_e32 v6, v6, v9
	s_addc_u32 s17, s10, 0
	v_lshlrev_b32_e32 v7, 3, v8
	v_lshlrev_b32_e32 v8, 5, v8
	v_ashrrev_i16_sdwa v6, v196, sext(v6) dst_sel:DWORD dst_unused:UNUSED_PAD src0_sel:DWORD src1_sel:BYTE_0
	v_readlane_b32 s11, v254, 8
	s_add_u32 s10, s7, s2
	v_and_b32_e32 v7, 0x3ffff0, v7
	v_and_b32_e32 v8, 32, v8
	v_bfe_i32 v6, v6, 0, 16
	s_addc_u32 s11, s17, s3
	s_add_i32 s20, 0, 0x10000
	s_lshl_b32 s2, s16, 18
	v_add_lshl_u32 v7, v10, v7, 10
	v_add_lshl_u32 v6, v8, v6, 1
	v_add_u32_e32 v204, s20, v5
	v_add3_u32 v209, v7, s2, v6
	v_mov_b32_e32 v202, 0x7a7a7a7a
	v_mov_b32_e32 v203, 0x7b7b7b7b
	v_mov_b32_e32 v6, v201
	v_readfirstlane_b32 s2, v204
	v_add_u32_e32 v205, 0x2000, v204
	s_mov_b32 m0, s2
	s_add_u32 s2, s10, 0x10000
	v_readfirstlane_b32 s19, v205
	global_load_lds_dwordx4 v6, s[10:11]
	s_addc_u32 s3, s11, 0
	v_mov_b32_e32 v6, v201
	s_mov_b32 m0, s19
	v_add_u32_e32 v208, 0, v5
	global_load_lds_dwordx4 v6, s[2:3]
	v_readlane_b32 s2, v253, 57
	v_mov_b32_e32 v6, v201
	v_add_u32_e32 v210, 0x10000, v209
	v_add_u32_e32 v206, s2, v5
	s_add_u32 s2, s10, 0x20000
	v_readfirstlane_b32 s19, v206
	s_addc_u32 s3, s11, 0
	s_mov_b32 m0, s19
	v_add_u32_e32 v207, 0x2000, v206
	global_load_lds_dwordx4 v6, s[2:3]
	s_add_u32 s2, s10, 0x30000
	v_mov_b32_e32 v6, v201
	v_readfirstlane_b32 s19, v207
	s_addc_u32 s3, s11, 0
	s_mov_b32 m0, s19
	v_add_u32_e32 v213, 0x2000, v208
	global_load_lds_dwordx4 v6, s[2:3]
	v_mov_b32_e32 v6, v209
	v_readfirstlane_b32 s2, v208
	s_mov_b32 m0, s2
	v_readfirstlane_b32 s2, v213
	global_load_lds_dwordx4 v6, s[8:9]
	v_mov_b32_e32 v6, v210
	v_add_u32_e32 v211, 0x20000, v209
	s_mov_b32 m0, s2
	v_add_u32_e32 v214, 0x4000, v208
	global_load_lds_dwordx4 v6, s[8:9]
	v_mov_b32_e32 v6, v211
	v_readfirstlane_b32 s2, v214
	v_add_u32_e32 v215, 0x6000, v208
	v_add_u32_e32 v212, 0x30000, v209
	s_mov_b32 m0, s2
	v_readfirstlane_b32 s2, v215
	global_load_lds_dwordx4 v6, s[8:9]
	v_mov_b32_e32 v6, v212
	s_mov_b32 m0, s2
	v_ashrrev_i32_e32 v4, 8, v2
	global_load_lds_dwordx4 v6, s[8:9]
	v_cmp_eq_u32_e64 s[36:37], 1, v4
	s_and_saveexec_b64 s[2:3], s[36:37]
	s_cbranch_execz .LBB0_1003
	s_barrier

.LBB0_1201:
	s_mov_b64 s[2:3], -1
	s_cmp_ge_u32 s10, s9
	s_mov_b64 s[6:7], -1
	s_cbranch_scc1 .LBB0_1200
	v_readlane_b32 s2, v255, 41
	v_readlane_b32 s6, v255, 40
	s_waitcnt lgkmcnt(0)
	s_lshr_b32 s2, s2, 16
	s_cmp_lg_u32 s2, 0
	s_cselect_b64 s[2:3], -1, 0
	s_cmp_lg_u64 s[2:3], 0
	s_addc_u32 s15, s6, s10
	s_and_b32 s13, s10, 7
	s_xor_b32 s3, s13, 7
	s_lshr_b32 s2, s10, 6
	s_add_i32 s3, s3, s8
	s_and_b32 s2, s2, 0x3fffff8
	s_ashr_i32 s6, s3, 3
	s_bfe_u32 s3, s10, 0x30003
	s_or_b32 s14, s3, s2
	s_cmp_lt_i32 s14, s6
	s_mov_b64 s[2:3], 0
	s_cselect_b64 s[6:7], -1, 0
	s_mov_b32 s10, s15
	s_branch .LBB0_1200

.LBB0_1231:
	v_readlane_b32 s2, v254, 3
	v_mov_b32_e32 v4, v0
	s_waitcnt lgkmcnt(0)
	v_mov_b32_e32 v2, s2
	s_barrier
	ds_read_b32 v2, v2
	v_readlane_b32 s2, v254, 7
	s_lshl_b32 s14, s2, 5
	v_readlane_b32 s18, v253, 0
	s_waitcnt lgkmcnt(0)
	v_readfirstlane_b32 s15, v2
	s_lshl_b32 s2, s15, 3
	s_addk_i32 s2, 0x1f8
	s_and_b32 s16, s2, 0xfffffe00
	s_cmp_ge_u32 s18, s16
	v_readfirstlane_b32 s26, v0
	v_readfirstlane_b32 s17, v0
	v_readlane_b32 s3, v254, 8
	s_cbranch_scc1 .LBB0_1243
	v_readlane_b32 s2, v255, 41
	v_readlane_b32 s4, v255, 40
	s_waitcnt lgkmcnt(0)
	s_lshr_b32 s2, s2, 16
	s_cmp_lg_u32 s2, 0
	s_cselect_b64 s[2:3], -1, 0
	s_cmp_lg_u64 s[2:3], 0
	s_addc_u32 s9, s4, 0
	s_branch .LBB0_1234

.LBB0_1250:
	v_readlane_b32 s2, v255, 41
	v_readlane_b32 s12, v255, 40
	s_waitcnt lgkmcnt(0)
	s_lshr_b32 s2, s2, 16
	s_cmp_lg_u32 s2, 0
	s_cselect_b64 s[2:3], -1, 0
	s_cmp_lg_u64 s[2:3], 0
	s_addc_u32 s33, s12, s18
	s_and_b32 s34, s18, 7
	s_xor_b32 s3, s34, 7
	s_lshr_b32 s2, s18, 6
	s_add_i32 s3, s3, s15
	s_and_b32 s2, s2, 0x3fffff8
	s_ashr_i32 s12, s3, 3
	s_bfe_u32 s3, s18, 0x30003
	s_or_b32 s35, s3, s2
	s_cmp_lt_i32 s35, s12
	s_mov_b64 s[2:3], 0
	s_cselect_b64 s[12:13], -1, 0

.LBB0_1369:
	s_or_b64 exec, exec, s[2:3]
	v_readlane_b32 s2, v254, 3
	v_mov_b32_e32 v4, v0
	s_waitcnt lgkmcnt(0)
	v_mov_b32_e32 v2, s2
	s_barrier
	ds_read_b32 v2, v2
	v_readlane_b32 s14, v253, 0
	v_readfirstlane_b32 s15, v0
	s_waitcnt lgkmcnt(0)
	v_readfirstlane_b32 s12, v2
	s_lshl_b32 s2, s12, 2
	s_addk_i32 s2, 0xfc
	s_and_b32 s13, s2, 0xffffff00
	s_cmp_ge_u32 s14, s13
	s_cbranch_scc1 .LBB0_1374
	v_readlane_b32 s2, v255, 41
	v_readlane_b32 s4, v255, 40
	s_waitcnt lgkmcnt(0)
	s_lshr_b32 s2, s2, 16
	s_cmp_lg_u32 s2, 0
	s_cselect_b64 s[2:3], -1, 0
	s_cmp_lg_u64 s[2:3], 0
	s_addc_u32 s9, s4, 0
	s_branch .LBB0_1372

.LBB0_1389:
	v_readlane_b32 s2, v255, 41
	v_readlane_b32 s10, v255, 40
	s_waitcnt lgkmcnt(0)
	s_lshr_b32 s2, s2, 16
	s_cmp_lg_u32 s2, 0
	s_cselect_b64 s[2:3], -1, 0
	s_cmp_lg_u64 s[2:3], 0
	s_addc_u32 s25, s10, s14
	s_and_b32 s26, s14, 7
	s_xor_b32 s3, s26, 7
	s_lshr_b32 s2, s14, 5
	s_add_i32 s3, s3, s12
	s_and_b32 s2, s2, 0x7fffff8
	s_ashr_i32 s10, s3, 3
	s_bfe_u32 s3, s14, 0x30003
	s_or_b32 s27, s3, s2
	s_cmp_lt_i32 s27, s10
	s_mov_b64 s[2:3], 0
	s_cselect_b64 s[10:11], -1, 0
